# P3: residual tile prefetched toward L2 or MALL by one dword LDS-DMA per trip during the K-loop (vmcnt recounted)
# baseline (speedup 1.0000x reference)
; #define PG8_STAGE(bufoff, gbase, voff) do { PG8_GLDS((const char*)(gbase), (voff)[0], ldsb + (bufoff)); PG8_GLDS((const char*)(gbase), (voff)[1], ldsb + (bufoff) + 8192u); } while (0)
; #define PG8_STAGEA(bufoff, gbase, o0, o1) do { PG8_GLDS((const char*)(gbase), (o0), ldsb + (bufoff)); PG8_GLDS((const char*)(gbase), (o1), ldsb + (bufoff) + 8192u); } while (0)
; #define PG8_STAGEA1(bufoff, gbase) do { if constexpr (Sched::GATHER) { PG8_STAGEA(bufoff, gbase, vA2, vA3); } else { PG8_STAGEA(bufoff, (gbase) + hstep, vA0, vA1); } } while (0)
; #define PG8_WAIT_L(n) asm volatile("s_waitcnt lgkmcnt(" #n ")" ::: "memory")
; template <class Epi, class Sched, bool F8 = false, bool PF = false, bool I8 = false, int PID = -1>
; __device__ __forceinline__ void gemm_phase(LAS unsigned char* lds, LAS unsigned char* xlds, const int RP, const int RPB, const int nt, const Sched& S, const Epi& E, const int stagger_ticks) {
;     ...
;         for (int t = 0; t < nt; t += 2) {
;             const bool last = (t == nt - 2);
;             unsigned ldsb = ldsb0; asm volatile("" : "+s"(ldsb));
;             const char* a1 = cA + (size_t)(t + 1) * kstep;
;             const char* a2 = last ? nA : cA + (size_t)(t + 2) * kstep; const char* b2 = last ? nB : cB + (size_t)(t + 2) * kstep;
;             const char* a3 = a2 + kstep; const char* b3 = b2 + kstep;
;             if constexpr (PF) { const char* pfa = (t + 4 < nt) ? cA + (size_t)(t + 4) * kstep : nA + (size_t)(t + 4 - nt) * kstep;
;                 asm volatile("s_mov_b32 m0, %2\n\ts_nop 0\n\tglobal_load_lds_dword %0, %1" :: "v"(voffP), "s"(pfa), "s"(ldsP) : "memory", "m0"); }
;             const bool relax = (Epi::RELAX > 0) && (t == 0) && epi_ran;
;             PG8_LDB(B0, 0, 0); PG8_LDB(B1, 0, 1); PG8_SCHED; PG8_LDA(At, 0, 0); PG8_STAGEA1(PG8_SA(1, 1), a1);
;             if (Sched::GATHER) { if (last) { const u32x4 nv = *nslot; vA0 = nv.x; vA1 = nv.y; vA2 = nv.z; vA3 = nv.w; } }
;             PG8_WAIT_VX(); PG8_WAIT_L(0); PG8_BAR; PG8_MMA(0, 0, At, B0); PG8_MMA(0, 1, At, B1); PG8_BAR; PG8_SCHED;
;             if constexpr (Epi::BIAS_DMA) { if (t == 0 && has_next) E.bias_dma(nxt, xlds + 8192 + ((ui + 1) & 1) * Epi::BIAS_STRIDE, wid, lane); }
;             PG8_LDA(At, 0, 1); PG8_STAGE(PG8_SB(0, 0), b2, voffB); PG8_STAGE(PG8_SB(0, 1), b2 + hstepB, voffB); PG8_STAGEA(PG8_SA(0, 0), a2, vA0, vA1);
.LBB0_546:
	s_mov_b64 s[36:37], s[10:11]
	s_add_u32 s20, s36, 0x100
	s_mov_b64 s[34:35], s[8:9]
	s_addc_u32 s45, s37, 0
	s_mov_b64 s[8:9], s[0:1]
	s_add_u32 s0, s34, 0x40080
	s_mov_b64 s[10:11], s[2:3]
	s_mov_b32 s15, s4
	s_mov_b32 s19, s6
	s_mov_b32 s6, s18
	s_mov_b32 s4, s14
	s_addc_u32 s1, s35, 0
	s_mov_b32 s46, -2
	v_and_b32_e32 v220, 63, v0
	v_lshrrev_b32_e32 v221, 5, v220
	v_lshlrev_b32_e32 v221, 2, v221
	v_and_b32_e32 v222, 7, v220
	v_lshl_add_u32 v221, v222, 7, v221
	v_bfe_u32 v222, v220, 3, 2
	v_lshl_add_u32 v220, v222, 12, v221
	s_lshl_b32 s98, s19, 20
	s_lshl_b32 s99, s15, 10
	s_add_u32 s98, s98, s99
	s_lshl_b32 s99, s93, 17
	s_add_u32 s98, s98, s99
	s_add_u32 s98, s16, s98
	s_addc_u32 s99, s17, 0
	s_lshl_b32 s100, s93, 8
	s_add_i32 s100, s100, 0x22800
.LBB0_547:
	s_mov_b32 s47, s5
	s_mov_b32 m0, s100
	s_nop 0
	global_load_lds_dword v220, s[98:99]
	s_add_u32 s98, s98, 0x4000
	s_addc_u32 s99, s99, 0
	v_add_u32_e32 v142, 0x10000, v195
	v_add_u32_e32 v158, 0x14000, v195
	ds_read_b128 v[130:133], v142
	ds_read_b128 v[134:137], v142 offset:1024
	ds_read_b128 v[138:141], v142 offset:2048
	ds_read_b128 v[142:145], v142 offset:3072
	ds_read_b128 v[146:149], v158
	ds_read_b128 v[150:153], v158 offset:1024
	ds_read_b128 v[154:157], v158 offset:2048
	ds_read_b128 v[158:161], v158 offset:3072
	s_add_u32 s2, s0, 0xfffc0080
	s_addc_u32 s3, s1, -1
	s_cmp_eq_u32 s46, 12
	s_cselect_b32 s36, s8, s2
	s_cselect_b32 s37, s9, s3
	s_cselect_b32 s34, s10, s20
	s_cselect_b32 s35, s11, s45
	s_add_u32 s2, s36, 0x80
	s_addc_u32 s3, s37, 0
	ds_read_b128 v[162:165], v196
	ds_read_b128 v[166:169], v196 offset:1024
	ds_read_b128 v[170:173], v196 offset:2048
	ds_read_b128 v[174:177], v196 offset:3072
	ds_read_b128 v[180:183], v196 offset:4096
	ds_read_b128 v[184:187], v196 offset:5120
	ds_read_b128 v[188:191], v196 offset:6144
	ds_read_b128 v[198:201], v196 offset:7168
	s_add_i32 s48, s47, 0xc000
	s_mov_b32 m0, s48
	s_nop 0
	global_load_lds_dwordx4 v1, s[0:1]
	s_add_i32 s48, s47, 0xe000
	s_mov_b32 m0, s48
	s_nop 0
	global_load_lds_dwordx4 v192, s[0:1]
	s_waitcnt vmcnt(9)
	s_waitcnt lgkmcnt(0)
	s_barrier
	s_setprio 1
	s_waitcnt lgkmcnt(7)
	v_mfma_f32_16x16x32_bf16 v[114:117], v[130:133], v[162:165], v[114:117]
	v_mfma_f32_16x16x32_bf16 v[118:121], v[138:141], v[162:165], v[118:121]
	s_waitcnt lgkmcnt(5)
	v_mfma_f32_16x16x32_bf16 v[110:113], v[130:133], v[170:173], v[110:113]
	v_mfma_f32_16x16x32_bf16 v[106:109], v[138:141], v[170:173], v[106:109]
	s_waitcnt lgkmcnt(3)
	v_mfma_f32_16x16x32_bf16 v[94:97], v[130:133], v[180:183], v[94:97]
	v_mfma_f32_16x16x32_bf16 v[90:93], v[138:141], v[180:183], v[90:93]
	s_waitcnt lgkmcnt(1)
	v_mfma_f32_16x16x32_bf16 v[78:81], v[130:133], v[188:191], v[78:81]
	v_mfma_f32_16x16x32_bf16 v[74:77], v[138:141], v[188:191], v[74:77]
	v_mfma_f32_16x16x32_bf16 v[114:117], v[134:137], v[166:169], v[114:117]
	v_mfma_f32_16x16x32_bf16 v[118:121], v[142:145], v[166:169], v[118:121]
	v_mfma_f32_16x16x32_bf16 v[110:113], v[134:137], v[174:177], v[110:113]
	v_mfma_f32_16x16x32_bf16 v[106:109], v[142:145], v[174:177], v[106:109]
	v_mfma_f32_16x16x32_bf16 v[94:97], v[134:137], v[184:187], v[94:97]
	v_mfma_f32_16x16x32_bf16 v[90:93], v[142:145], v[184:187], v[90:93]
	s_waitcnt lgkmcnt(0)
	v_mfma_f32_16x16x32_bf16 v[78:81], v[134:137], v[198:201], v[78:81]
	v_mfma_f32_16x16x32_bf16 v[74:77], v[142:145], v[198:201], v[74:77]
	s_setprio 0
	s_setprio 1
	v_mfma_f32_16x16x32_bf16 v[126:129], v[146:149], v[162:165], v[126:129]
	v_mfma_f32_16x16x32_bf16 v[122:125], v[154:157], v[162:165], v[122:125]
	v_mfma_f32_16x16x32_bf16 v[102:105], v[146:149], v[170:173], v[102:105]
	v_mfma_f32_16x16x32_bf16 v[98:101], v[154:157], v[170:173], v[98:101]
	v_mfma_f32_16x16x32_bf16 v[86:89], v[146:149], v[180:183], v[86:89]
	v_mfma_f32_16x16x32_bf16 v[82:85], v[154:157], v[180:183], v[82:85]
	v_mfma_f32_16x16x32_bf16 v[70:73], v[146:149], v[188:191], v[70:73]
	v_mfma_f32_16x16x32_bf16 v[66:69], v[154:157], v[188:191], v[66:69]
	v_mfma_f32_16x16x32_bf16 v[126:129], v[150:153], v[166:169], v[126:129]
	v_mfma_f32_16x16x32_bf16 v[122:125], v[158:161], v[166:169], v[122:125]
	v_mfma_f32_16x16x32_bf16 v[102:105], v[150:153], v[174:177], v[102:105]
	v_mfma_f32_16x16x32_bf16 v[98:101], v[158:161], v[174:177], v[98:101]
	v_mfma_f32_16x16x32_bf16 v[86:89], v[150:153], v[184:187], v[86:89]
	v_mfma_f32_16x16x32_bf16 v[82:85], v[158:161], v[184:187], v[82:85]
	v_mfma_f32_16x16x32_bf16 v[70:73], v[150:153], v[198:201], v[70:73]
	v_mfma_f32_16x16x32_bf16 v[66:69], v[158:161], v[198:201], v[66:69]
	s_setprio 0
	s_barrier
	ds_read_b128 v[162:165], v196 offset:16384
	ds_read_b128 v[166:169], v196 offset:17408
	ds_read_b128 v[170:173], v196 offset:18432
	ds_read_b128 v[174:177], v196 offset:19456
	ds_read_b128 v[180:183], v196 offset:20480
	ds_read_b128 v[184:187], v196 offset:21504
	ds_read_b128 v[188:191], v196 offset:22528
	ds_read_b128 v[198:201], v196 offset:23552
	s_add_i32 s48, s47, 0x10000
	s_mov_b32 m0, s48
	s_nop 0
	global_load_lds_dwordx4 v193, s[34:35]
	s_add_i32 s48, s47, 0x12000
	s_mov_b32 m0, s48
	s_nop 0
	global_load_lds_dwordx4 v194, s[34:35]
	s_add_u32 s48, s34, 0x4000
	s_addc_u32 s49, s35, 0
	s_add_i32 s50, s47, 0x14000
	s_mov_b32 m0, s50
	s_nop 0
	global_load_lds_dwordx4 v193, s[48:49]
	s_add_i32 s50, s47, 0x16000
	s_mov_b32 m0, s50
	s_nop 0
	global_load_lds_dwordx4 v194, s[48:49]
	s_add_i32 s48, s47, 0x2000
	s_mov_b32 m0, s47
	s_nop 0
	global_load_lds_dwordx4 v1, s[36:37]
	s_nop 0
	s_mov_b32 m0, s48
	s_nop 0
	global_load_lds_dwordx4 v192, s[36:37]
	s_waitcnt vmcnt(9)
	s_waitcnt lgkmcnt(0)
	s_barrier
; #define PG8_STAGE(bufoff, gbase, voff) do { PG8_GLDS((const char*)(gbase), (voff)[0], ldsb + (bufoff)); PG8_GLDS((const char*)(gbase), (voff)[1], ldsb + (bufoff) + 8192u); } while (0)
; #define PG8_STAGEA(bufoff, gbase, o0, o1) do { PG8_GLDS((const char*)(gbase), (o0), ldsb + (bufoff)); PG8_GLDS((const char*)(gbase), (o1), ldsb + (bufoff) + 8192u); } while (0)
; #define PG8_STAGEA1(bufoff, gbase) do { if constexpr (Sched::GATHER) { PG8_STAGEA(bufoff, gbase, vA2, vA3); } else { PG8_STAGEA(bufoff, (gbase) + hstep, vA0, vA1); } } while (0)
; #define PG8_LDA(dst, b, h) do { if constexpr (F8) { _Pragma("unroll") for (int m = 0; m < 4; ++m) dst##8[m] = PG8_LD32(lds + PG8_SA(b, h) + aoff + m * 2048); } else { \
;         _Pragma("unroll") for (int m = 0; m < 4; ++m) _Pragma("unroll") for (int k = 0; k < 2; ++k) dst[m][k] = *(const LAS bf16x8*)(lds + PG8_SA(b, h) + aoff + m * 2048 + k * 1024); } } while (0)
; #define PG8_LDB(dst, b, h) do { if constexpr (F8) { _Pragma("unroll") for (int n = 0; n < 2; ++n) dst##8[n] = PG8_LD32(lds + PG8_SB(b, h) + boff + n * 2048); } else { \
;         _Pragma("unroll") for (int n = 0; n < 2; ++n) _Pragma("unroll") for (int k = 0; k < 2; ++k) dst[n][k] = *(const LAS bf16x8*)(lds + PG8_SB(b, h) + boff + n * 2048 + k * 1024); } } while (0)
; #define PG8_WAIT_VR() PG8_WAIT_V(8)
; #define PG8_WAIT_VX() do { if (relax) asm volatile("s_waitcnt vmcnt(%0)" :: "n"(8 + Epi::RELAX) : "memory"); else PG8_WAIT_V(8); } while (0)
; #define PG8_WAIT_L(n) asm volatile("s_waitcnt lgkmcnt(" #n ")" ::: "memory")
; #define PG8_BAR __builtin_amdgcn_s_barrier()
; template <class Epi, class Sched, bool F8 = false, bool PF = false, bool I8 = false, int PID = -1>
; __device__ __forceinline__ void gemm_phase(LAS unsigned char* lds, LAS unsigned char* xlds, const int RP, const int RPB, const int nt, const Sched& S, const Epi& E, const int stagger_ticks) {
;     ...
;             PG8_WAIT_VX(); PG8_WAIT_L(0); PG8_BAR; PG8_MMA(1, 0, At, B0); PG8_MMA(1, 1, At, B1); PG8_BAR; PG8_SCHED;
;             PG8_LDB(B0, 1, 0); PG8_LDB(B1, 1, 1); PG8_SCHED; PG8_LDA(At, 1, 0); PG8_STAGEA1(PG8_SA(0, 1), a2);
;             PG8_WAIT_VR(); PG8_WAIT_L(0); PG8_BAR; PG8_MMA(0, 0, At, B0); PG8_MMA(0, 1, At, B1); PG8_BAR; PG8_SCHED;
;             PG8_LDA(At, 1, 1); PG8_STAGE(PG8_SB(1, 0), b3, voffB); PG8_STAGE(PG8_SB(1, 1), b3 + hstepB, voffB); PG8_STAGEA(PG8_SA(1, 0), a3, vA0, vA1);
	s_setprio 1
	s_waitcnt lgkmcnt(7)
	v_mfma_f32_16x16x32_bf16 v[50:53], v[130:133], v[162:165], v[50:53]
	v_mfma_f32_16x16x32_bf16 v[54:57], v[138:141], v[162:165], v[54:57]
	s_waitcnt lgkmcnt(5)
	v_mfma_f32_16x16x32_bf16 v[46:49], v[130:133], v[170:173], v[46:49]
	v_mfma_f32_16x16x32_bf16 v[42:45], v[138:141], v[170:173], v[42:45]
	s_waitcnt lgkmcnt(3)
	v_mfma_f32_16x16x32_bf16 v[30:33], v[130:133], v[180:183], v[30:33]
	v_mfma_f32_16x16x32_bf16 v[26:29], v[138:141], v[180:183], v[26:29]
	s_waitcnt lgkmcnt(1)
	v_mfma_f32_16x16x32_bf16 v[14:17], v[130:133], v[188:191], v[14:17]
	v_mfma_f32_16x16x32_bf16 v[10:13], v[138:141], v[188:191], v[10:13]
	v_mfma_f32_16x16x32_bf16 v[50:53], v[134:137], v[166:169], v[50:53]
	v_mfma_f32_16x16x32_bf16 v[54:57], v[142:145], v[166:169], v[54:57]
	v_mfma_f32_16x16x32_bf16 v[46:49], v[134:137], v[174:177], v[46:49]
	v_mfma_f32_16x16x32_bf16 v[42:45], v[142:145], v[174:177], v[42:45]
	v_mfma_f32_16x16x32_bf16 v[30:33], v[134:137], v[184:187], v[30:33]
	v_mfma_f32_16x16x32_bf16 v[26:29], v[142:145], v[184:187], v[26:29]
	s_waitcnt lgkmcnt(0)
	v_mfma_f32_16x16x32_bf16 v[14:17], v[134:137], v[198:201], v[14:17]
	v_mfma_f32_16x16x32_bf16 v[10:13], v[142:145], v[198:201], v[10:13]
	s_setprio 0
	s_setprio 1
	v_mfma_f32_16x16x32_bf16 v[58:61], v[146:149], v[162:165], v[58:61]
	v_mfma_f32_16x16x32_bf16 v[62:65], v[154:157], v[162:165], v[62:65]
	v_mfma_f32_16x16x32_bf16 v[38:41], v[146:149], v[170:173], v[38:41]
	v_mfma_f32_16x16x32_bf16 v[34:37], v[154:157], v[170:173], v[34:37]
	v_mfma_f32_16x16x32_bf16 v[22:25], v[146:149], v[180:183], v[22:25]
	v_mfma_f32_16x16x32_bf16 v[18:21], v[154:157], v[180:183], v[18:21]
	v_mfma_f32_16x16x32_bf16 v[6:9], v[146:149], v[188:191], v[6:9]
	v_mfma_f32_16x16x32_bf16 v[2:5], v[154:157], v[188:191], v[2:5]
	v_mfma_f32_16x16x32_bf16 v[58:61], v[150:153], v[166:169], v[58:61]
	v_mfma_f32_16x16x32_bf16 v[62:65], v[158:161], v[166:169], v[62:65]
	v_mfma_f32_16x16x32_bf16 v[38:41], v[150:153], v[174:177], v[38:41]
	v_mfma_f32_16x16x32_bf16 v[34:37], v[158:161], v[174:177], v[34:37]
	v_mfma_f32_16x16x32_bf16 v[22:25], v[150:153], v[184:187], v[22:25]
	v_mfma_f32_16x16x32_bf16 v[18:21], v[158:161], v[184:187], v[18:21]
	v_mfma_f32_16x16x32_bf16 v[6:9], v[150:153], v[198:201], v[6:9]
	v_mfma_f32_16x16x32_bf16 v[2:5], v[158:161], v[198:201], v[2:5]
	s_setprio 0
	s_barrier
	v_add_u32_e32 v142, 0x18000, v195
	v_add_u32_e32 v158, 0x1c000, v195
	ds_read_b128 v[130:133], v142
	ds_read_b128 v[134:137], v142 offset:1024
	ds_read_b128 v[138:141], v142 offset:2048
	ds_read_b128 v[142:145], v142 offset:3072
	ds_read_b128 v[146:149], v158
	ds_read_b128 v[150:153], v158 offset:1024
	ds_read_b128 v[154:157], v158 offset:2048
	ds_read_b128 v[158:161], v158 offset:3072
	ds_read_b128 v[162:165], v196 offset:32768
	ds_read_b128 v[166:169], v196 offset:33792
	ds_read_b128 v[170:173], v196 offset:34816
	ds_read_b128 v[174:177], v196 offset:35840
	ds_read_b128 v[180:183], v196 offset:36864
	ds_read_b128 v[184:187], v196 offset:37888
	ds_read_b128 v[188:191], v196 offset:38912
	ds_read_b128 v[198:201], v196 offset:39936
	s_add_u32 s36, s36, 0x40000
	s_addc_u32 s37, s37, 0
	s_add_i32 s48, s47, 0x4000
	s_mov_b32 m0, s48
	s_nop 0
	global_load_lds_dwordx4 v1, s[36:37]
	s_add_i32 s48, s47, 0x6000
	s_mov_b32 m0, s48
	s_nop 0
	global_load_lds_dwordx4 v192, s[36:37]
	s_waitcnt vmcnt(8)
	s_waitcnt lgkmcnt(0)
	s_barrier
	s_setprio 1
	s_waitcnt lgkmcnt(7)
	v_mfma_f32_16x16x32_bf16 v[114:117], v[130:133], v[162:165], v[114:117]
	v_mfma_f32_16x16x32_bf16 v[118:121], v[138:141], v[162:165], v[118:121]
	s_waitcnt lgkmcnt(5)
	v_mfma_f32_16x16x32_bf16 v[110:113], v[130:133], v[170:173], v[110:113]
	v_mfma_f32_16x16x32_bf16 v[106:109], v[138:141], v[170:173], v[106:109]
	s_waitcnt lgkmcnt(3)
	v_mfma_f32_16x16x32_bf16 v[94:97], v[130:133], v[180:183], v[94:97]
	v_mfma_f32_16x16x32_bf16 v[90:93], v[138:141], v[180:183], v[90:93]
	s_waitcnt lgkmcnt(1)
	v_mfma_f32_16x16x32_bf16 v[78:81], v[130:133], v[188:191], v[78:81]
	v_mfma_f32_16x16x32_bf16 v[74:77], v[138:141], v[188:191], v[74:77]
	v_mfma_f32_16x16x32_bf16 v[114:117], v[134:137], v[166:169], v[114:117]
	v_mfma_f32_16x16x32_bf16 v[118:121], v[142:145], v[166:169], v[118:121]
	v_mfma_f32_16x16x32_bf16 v[110:113], v[134:137], v[174:177], v[110:113]
	v_mfma_f32_16x16x32_bf16 v[106:109], v[142:145], v[174:177], v[106:109]
	v_mfma_f32_16x16x32_bf16 v[94:97], v[134:137], v[184:187], v[94:97]
	v_mfma_f32_16x16x32_bf16 v[90:93], v[142:145], v[184:187], v[90:93]
	s_waitcnt lgkmcnt(0)
	v_mfma_f32_16x16x32_bf16 v[78:81], v[134:137], v[198:201], v[78:81]
	v_mfma_f32_16x16x32_bf16 v[74:77], v[142:145], v[198:201], v[74:77]
	s_setprio 0
	s_setprio 1
	v_mfma_f32_16x16x32_bf16 v[126:129], v[146:149], v[162:165], v[126:129]
	v_mfma_f32_16x16x32_bf16 v[122:125], v[154:157], v[162:165], v[122:125]
	v_mfma_f32_16x16x32_bf16 v[102:105], v[146:149], v[170:173], v[102:105]
	v_mfma_f32_16x16x32_bf16 v[98:101], v[154:157], v[170:173], v[98:101]
	v_mfma_f32_16x16x32_bf16 v[86:89], v[146:149], v[180:183], v[86:89]
	v_mfma_f32_16x16x32_bf16 v[82:85], v[154:157], v[180:183], v[82:85]
	v_mfma_f32_16x16x32_bf16 v[70:73], v[146:149], v[188:191], v[70:73]
	v_mfma_f32_16x16x32_bf16 v[66:69], v[154:157], v[188:191], v[66:69]
	v_mfma_f32_16x16x32_bf16 v[126:129], v[150:153], v[166:169], v[126:129]
	v_mfma_f32_16x16x32_bf16 v[122:125], v[158:161], v[166:169], v[122:125]
	v_mfma_f32_16x16x32_bf16 v[102:105], v[150:153], v[174:177], v[102:105]
	v_mfma_f32_16x16x32_bf16 v[98:101], v[158:161], v[174:177], v[98:101]
	v_mfma_f32_16x16x32_bf16 v[86:89], v[150:153], v[184:187], v[86:89]
	v_mfma_f32_16x16x32_bf16 v[82:85], v[158:161], v[184:187], v[82:85]
	v_mfma_f32_16x16x32_bf16 v[70:73], v[150:153], v[198:201], v[70:73]
	v_mfma_f32_16x16x32_bf16 v[66:69], v[158:161], v[198:201], v[66:69]
	s_setprio 0
	s_barrier
; #define PG8_STAGE(bufoff, gbase, voff) do { PG8_GLDS((const char*)(gbase), (voff)[0], ldsb + (bufoff)); PG8_GLDS((const char*)(gbase), (voff)[1], ldsb + (bufoff) + 8192u); } while (0)
; #define PG8_STAGEA(bufoff, gbase, o0, o1) do { PG8_GLDS((const char*)(gbase), (o0), ldsb + (bufoff)); PG8_GLDS((const char*)(gbase), (o1), ldsb + (bufoff) + 8192u); } while (0)
; #define PG8_LDA(dst, b, h) do { if constexpr (F8) { _Pragma("unroll") for (int m = 0; m < 4; ++m) dst##8[m] = PG8_LD32(lds + PG8_SA(b, h) + aoff + m * 2048); } else { \
;         _Pragma("unroll") for (int m = 0; m < 4; ++m) _Pragma("unroll") for (int k = 0; k < 2; ++k) dst[m][k] = *(const LAS bf16x8*)(lds + PG8_SA(b, h) + aoff + m * 2048 + k * 1024); } } while (0)
; #define PG8_WAIT_VR() PG8_WAIT_V(8)
; #define PG8_WAIT_L(n) asm volatile("s_waitcnt lgkmcnt(" #n ")" ::: "memory")
; #define PG8_BAR __builtin_amdgcn_s_barrier()
; #define PG8_SCHED __builtin_amdgcn_sched_barrier(0)
; #define PROF_BEGIN(sel) do { if constexpr (PROF && PROF_SEL == (sel)) prof_t0 = (unsigned)__builtin_amdgcn_s_memrealtime(); } while (0)
; #define PROF_END(sel) do { if constexpr (PROF && PROF_SEL == (sel)) prof_acc += (unsigned)__builtin_amdgcn_s_memrealtime() - prof_t0; } while (0)
;     __device__ __forceinline__ bool next(int i, pg8::Unit& u) const { const int L = i * G + c; if (L >= nM * 4) return false; int pm, pn; pg8::tile_remap<4>(L, nM, pm, pn); if (rev) pm = nM - 1 - pm; u.pm = pm; u.pn = pn; u.aux = 0; u.skip = 0; return true; }
; template <class Epi, class Sched, bool F8 = false, bool PF = false, bool I8 = false, int PID = -1>
; __device__ __forceinline__ void gemm_phase(LAS unsigned char* lds, LAS unsigned char* xlds, const int RP, const int RPB, const int nt, const Sched& S, const Epi& E, const int stagger_ticks) {
;     ...
;             PG8_LDA(At, 1, 1); PG8_STAGE(PG8_SB(1, 0), b3, voffB); PG8_STAGE(PG8_SB(1, 1), b3 + hstepB, voffB); PG8_STAGEA(PG8_SA(1, 0), a3, vA0, vA1);
;             PG8_WAIT_VR(); PG8_WAIT_L(0); PG8_BAR; PG8_MMA(1, 0, At, B0); PG8_MMA(1, 1, At, B1); PG8_BAR; PG8_SCHED;
;         }
;         PROF_END(1); PROF_BEGIN(3);
;         if (wr == 0) PG8_BAR;
;         Unit nn; bool has_nn = false; unsigned gv[4] = {vA0, vA1, vA2, vA3};
;         if (has_next) { has_nn = S.next(ui + 2, nn); if (Sched::GATHER) { if (has_nn) S.a_offsets(nn, Rr, Cc, RP, gv); } }
	s_add_u32 s36, s34, 0x80
	ds_read_b128 v[162:165], v196 offset:49152
	ds_read_b128 v[166:169], v196 offset:50176
	ds_read_b128 v[170:173], v196 offset:51200
	ds_read_b128 v[174:177], v196 offset:52224
	ds_read_b128 v[180:183], v196 offset:53248
	ds_read_b128 v[184:187], v196 offset:54272
	ds_read_b128 v[188:191], v196 offset:55296
	ds_read_b128 v[198:201], v196 offset:56320
	s_addc_u32 s37, s35, 0
	s_add_i32 s48, s47, 0x18000
	s_mov_b32 m0, s48
	s_nop 0
	global_load_lds_dwordx4 v193, s[36:37]
	s_add_i32 s48, s47, 0x1a000
	s_mov_b32 m0, s48
	s_nop 0
	global_load_lds_dwordx4 v194, s[36:37]
	s_add_u32 s34, s34, 0x4080
	s_addc_u32 s35, s35, 0
	s_add_i32 s36, s47, 0x1c000
	s_mov_b32 m0, s36
	s_nop 0
	global_load_lds_dwordx4 v193, s[34:35]
	s_add_i32 s36, s47, 0x1e000
	s_mov_b32 m0, s36
	s_nop 0
	global_load_lds_dwordx4 v194, s[34:35]
	s_add_i32 s34, s47, 0x8000
	s_mov_b32 m0, s34
	s_nop 0
	global_load_lds_dwordx4 v1, s[2:3]
	s_add_i32 s47, s47, 0xa000
	s_mov_b32 m0, s47
	s_nop 0
	global_load_lds_dwordx4 v192, s[2:3]
	s_waitcnt vmcnt(8)
	s_waitcnt lgkmcnt(0)
	s_barrier
	s_setprio 1
	s_waitcnt lgkmcnt(7)
	v_mfma_f32_16x16x32_bf16 v[50:53], v[130:133], v[162:165], v[50:53]
	v_mfma_f32_16x16x32_bf16 v[54:57], v[138:141], v[162:165], v[54:57]
	s_waitcnt lgkmcnt(5)
	v_mfma_f32_16x16x32_bf16 v[46:49], v[130:133], v[170:173], v[46:49]
	v_mfma_f32_16x16x32_bf16 v[42:45], v[138:141], v[170:173], v[42:45]
	s_waitcnt lgkmcnt(3)
	v_mfma_f32_16x16x32_bf16 v[30:33], v[130:133], v[180:183], v[30:33]
	v_mfma_f32_16x16x32_bf16 v[26:29], v[138:141], v[180:183], v[26:29]
	s_waitcnt lgkmcnt(1)
	v_mfma_f32_16x16x32_bf16 v[14:17], v[130:133], v[188:191], v[14:17]
	v_mfma_f32_16x16x32_bf16 v[10:13], v[138:141], v[188:191], v[10:13]
	v_mfma_f32_16x16x32_bf16 v[50:53], v[134:137], v[166:169], v[50:53]
	v_mfma_f32_16x16x32_bf16 v[54:57], v[142:145], v[166:169], v[54:57]
	v_mfma_f32_16x16x32_bf16 v[46:49], v[134:137], v[174:177], v[46:49]
	v_mfma_f32_16x16x32_bf16 v[42:45], v[142:145], v[174:177], v[42:45]
	v_mfma_f32_16x16x32_bf16 v[30:33], v[134:137], v[184:187], v[30:33]
	v_mfma_f32_16x16x32_bf16 v[26:29], v[142:145], v[184:187], v[26:29]
	s_waitcnt lgkmcnt(0)
	v_mfma_f32_16x16x32_bf16 v[14:17], v[134:137], v[198:201], v[14:17]
	v_mfma_f32_16x16x32_bf16 v[10:13], v[142:145], v[198:201], v[10:13]
	s_setprio 0
	s_setprio 1
	v_mfma_f32_16x16x32_bf16 v[58:61], v[146:149], v[162:165], v[58:61]
	v_mfma_f32_16x16x32_bf16 v[62:65], v[154:157], v[162:165], v[62:65]
	v_mfma_f32_16x16x32_bf16 v[38:41], v[146:149], v[170:173], v[38:41]
	v_mfma_f32_16x16x32_bf16 v[34:37], v[154:157], v[170:173], v[34:37]
	v_mfma_f32_16x16x32_bf16 v[22:25], v[146:149], v[180:183], v[22:25]
	v_mfma_f32_16x16x32_bf16 v[18:21], v[154:157], v[180:183], v[18:21]
	v_mfma_f32_16x16x32_bf16 v[6:9], v[146:149], v[188:191], v[6:9]
	v_mfma_f32_16x16x32_bf16 v[2:5], v[154:157], v[188:191], v[2:5]
	v_mfma_f32_16x16x32_bf16 v[58:61], v[150:153], v[166:169], v[58:61]
	v_mfma_f32_16x16x32_bf16 v[62:65], v[158:161], v[166:169], v[62:65]
	v_mfma_f32_16x16x32_bf16 v[38:41], v[150:153], v[174:177], v[38:41]
	v_mfma_f32_16x16x32_bf16 v[34:37], v[158:161], v[174:177], v[34:37]
	v_mfma_f32_16x16x32_bf16 v[22:25], v[150:153], v[184:187], v[22:25]
	v_mfma_f32_16x16x32_bf16 v[18:21], v[158:161], v[184:187], v[18:21]
	v_mfma_f32_16x16x32_bf16 v[6:9], v[150:153], v[198:201], v[6:9]
	v_mfma_f32_16x16x32_bf16 v[2:5], v[158:161], v[198:201], v[2:5]
	s_setprio 0
	s_barrier
	s_add_i32 s46, s46, 2
	s_add_u32 s20, s20, 0x100
	s_addc_u32 s45, s45, 0
	s_add_u32 s0, s0, 0x100
	s_addc_u32 s1, s1, 0
	s_cmp_gt_u32 s46, 13
	s_cbranch_scc0 .LBB0_547
	s_and_b64 vcc, exec, s[30:31]
	s_cbranch_vccz .LBB0_550
	s_barrier
